# reduce_slabs: non-temporal slab loads (read once), on top of prep_all nt input loads
# baseline (speedup 1.0000x reference)
.Lrs_nocs:
	s_or_b64 exec, exec, s[16:17]
	s_add_u32 s4, s4, s8
	s_addc_u32 s5, s5, s9
	v_lshlrev_b32_e32 v20, 4, v1
	v_mov_b32_e32 v21, 0
	v_lshl_add_u64 v[4:5], s[4:5], 0, v[20:21]
	s_mov_b32 s8, 0x400000
	v_add_co_u32_e32 v12, vcc, s8, v4
	s_lshl_b64 s[2:3], s[2:3], 21
	s_nop 0
	v_addc_co_u32_e32 v13, vcc, 0, v5, vcc
	global_load_dwordx4 v[4:7], v20, s[4:5] nt
	global_load_dwordx4 v[8:11], v[12:13], off nt
	s_add_u32 s2, s6, s2
	v_lshlrev_b32_e32 v1, 3, v1
	s_addc_u32 s3, s7, s3
	s_waitcnt vmcnt(0)
	v_pk_add_f32 v[4:5], v[4:5], v[8:9]
	v_pk_add_f32 v[6:7], v[6:7], v[10:11]
	v_cvt_pk_f16_f32 v4, v4, v5
	v_cvt_pk_f16_f32 v5, v6, v7
	global_store_dwordx2 v1, v[4:5], s[2:3]
	v_cmp_gt_i32_e32 vcc, s11, v2
	s_and_saveexec_b64 s[2:3], vcc
	s_cbranch_execz .LBB1_2
	v_add_f32_e32 v0, 0, v40
	v_add_f32_e32 v0, v0, v41
	v_add_f32_e32 v0, v0, v42
	v_add_f32_e32 v0, v0, v43
	v_add_f32_e32 v0, v0, v44
	v_add_f32_e32 v0, v0, v45
	v_add_f32_e32 v0, v0, v46
	v_add_f32_e32 v0, v0, v47
	v_add_f32_e32 v0, v0, v48
	v_add_f32_e32 v0, v0, v49
	v_add_f32_e32 v0, v0, v50
	v_add_f32_e32 v0, v0, v51
	v_add_f32_e32 v0, v0, v52
	v_add_f32_e32 v0, v0, v53
	v_add_f32_e32 v0, v0, v54
	v_add_f32_e32 v4, v0, v55
	v_ashrrev_i32_e32 v3, 31, v2
	v_lshl_add_u64 v[0:1], v[2:3], 2, s[14:15]
	global_store_dword v[0:1], v4, off
